# baseline (speedup 1.0000x reference)
.Lg0_cloop:
	s_mul_i32 s8, s3, 0x7000
	s_barrier
	v_add_u32_e32 v103, s8, v100
	v_add_u32_e32 v101, s8, v99
	ds_read_b128 v[146:149], v103 offset:12288
	ds_read_b128 v[150:153], v103 offset:13312
	ds_read_b128 v[154:157], v103 offset:14336
	ds_read_b128 v[158:161], v103 offset:15360
	s_waitcnt lgkmcnt(9)
	v_mfma_f32_16x16x32_f16 v[94:97], v[122:125], v[104:107], v[94:97]
	s_add_i32 s8, s3, 1
	s_cmp_lg_u32 s3, 4
	s_cselect_b32 s3, s8, 0
	v_mfma_f32_16x16x32_f16 v[70:73], v[122:125], v[108:111], v[70:73]
	v_mfma_f32_16x16x32_f16 v[46:49], v[122:125], v[112:115], v[46:49]
	v_mfma_f32_16x16x32_f16 v[22:25], v[122:125], v[116:119], v[22:25]
	ds_read_b128 v[122:125], v101
	s_waitcnt lgkmcnt(9)
	v_mfma_f32_16x16x32_f16 v[90:93], v[126:129], v[104:107], v[90:93]
	v_mfma_f32_16x16x32_f16 v[66:69], v[126:129], v[108:111], v[66:69]
	v_mfma_f32_16x16x32_f16 v[42:45], v[126:129], v[112:115], v[42:45]
	v_mfma_f32_16x16x32_f16 v[18:21], v[126:129], v[116:119], v[18:21]
	ds_read_b128 v[126:129], v101 offset:1024
	s_waitcnt lgkmcnt(9)
	v_mfma_f32_16x16x32_f16 v[86:89], v[130:133], v[104:107], v[86:89]
	v_mfma_f32_16x16x32_f16 v[54:57], v[130:133], v[108:111], v[54:57]
	v_mfma_f32_16x16x32_f16 v[26:29], v[130:133], v[112:115], v[26:29]
	v_mfma_f32_16x16x32_f16 v[6:9], v[130:133], v[116:119], v[6:9]
	ds_read_b128 v[130:133], v101 offset:2048
	s_waitcnt lgkmcnt(9)
	v_mfma_f32_16x16x32_f16 v[74:77], v[134:137], v[104:107], v[74:77]
	v_mfma_f32_16x16x32_f16 v[50:53], v[134:137], v[108:111], v[50:53]
	v_mfma_f32_16x16x32_f16 v[38:41], v[134:137], v[112:115], v[38:41]
	v_mfma_f32_16x16x32_f16 v[14:17], v[134:137], v[116:119], v[14:17]
	ds_read_b128 v[134:137], v101 offset:3072
	s_waitcnt lgkmcnt(9)
	v_mfma_f32_16x16x32_f16 v[82:85], v[138:141], v[104:107], v[82:85]
	v_mfma_f32_16x16x32_f16 v[58:61], v[138:141], v[108:111], v[58:61]
	v_mfma_f32_16x16x32_f16 v[30:33], v[138:141], v[112:115], v[30:33]
	v_mfma_f32_16x16x32_f16 v[10:13], v[138:141], v[116:119], v[10:13]
	ds_read_b128 v[138:141], v101 offset:4096
	s_waitcnt lgkmcnt(9)
	v_mfma_f32_16x16x32_f16 v[78:81], v[142:145], v[104:107], v[78:81]
	v_mfma_f32_16x16x32_f16 v[62:65], v[142:145], v[108:111], v[62:65]
	v_mfma_f32_16x16x32_f16 v[34:37], v[142:145], v[112:115], v[34:37]
	v_mfma_f32_16x16x32_f16 v[2:5], v[142:145], v[116:119], v[2:5]
	ds_read_b128 v[142:145], v101 offset:5120
	s_mul_i32 s8, s3, 0x7000
	s_barrier
	v_add_u32_e32 v103, s8, v100
	v_add_u32_e32 v101, s8, v99
	ds_read_b128 v[104:107], v103 offset:12288
	ds_read_b128 v[108:111], v103 offset:13312
	ds_read_b128 v[112:115], v103 offset:14336
	ds_read_b128 v[116:119], v103 offset:15360
	s_waitcnt lgkmcnt(9)
	v_mfma_f32_16x16x32_f16 v[94:97], v[122:125], v[146:149], v[94:97]
	s_add_i32 s8, s3, 1
	s_cmp_lg_u32 s3, 4
	s_cselect_b32 s3, s8, 0
	v_mfma_f32_16x16x32_f16 v[70:73], v[122:125], v[150:153], v[70:73]
	v_mfma_f32_16x16x32_f16 v[46:49], v[122:125], v[154:157], v[46:49]
	v_mfma_f32_16x16x32_f16 v[22:25], v[122:125], v[158:161], v[22:25]
	ds_read_b128 v[122:125], v101
	s_waitcnt lgkmcnt(9)
	v_mfma_f32_16x16x32_f16 v[90:93], v[126:129], v[146:149], v[90:93]
	v_mfma_f32_16x16x32_f16 v[66:69], v[126:129], v[150:153], v[66:69]
	v_mfma_f32_16x16x32_f16 v[42:45], v[126:129], v[154:157], v[42:45]
	v_mfma_f32_16x16x32_f16 v[18:21], v[126:129], v[158:161], v[18:21]
	ds_read_b128 v[126:129], v101 offset:1024
	s_waitcnt lgkmcnt(9)
	v_mfma_f32_16x16x32_f16 v[86:89], v[130:133], v[146:149], v[86:89]
	v_mfma_f32_16x16x32_f16 v[54:57], v[130:133], v[150:153], v[54:57]
	v_mfma_f32_16x16x32_f16 v[26:29], v[130:133], v[154:157], v[26:29]
	v_mfma_f32_16x16x32_f16 v[6:9], v[130:133], v[158:161], v[6:9]
	ds_read_b128 v[130:133], v101 offset:2048
	s_waitcnt lgkmcnt(9)
	v_mfma_f32_16x16x32_f16 v[74:77], v[134:137], v[146:149], v[74:77]
	v_mfma_f32_16x16x32_f16 v[50:53], v[134:137], v[150:153], v[50:53]
	v_mfma_f32_16x16x32_f16 v[38:41], v[134:137], v[154:157], v[38:41]
	v_mfma_f32_16x16x32_f16 v[14:17], v[134:137], v[158:161], v[14:17]
	ds_read_b128 v[134:137], v101 offset:3072
	s_waitcnt lgkmcnt(9)
	v_mfma_f32_16x16x32_f16 v[82:85], v[138:141], v[146:149], v[82:85]
	v_mfma_f32_16x16x32_f16 v[58:61], v[138:141], v[150:153], v[58:61]
	v_mfma_f32_16x16x32_f16 v[30:33], v[138:141], v[154:157], v[30:33]
	v_mfma_f32_16x16x32_f16 v[10:13], v[138:141], v[158:161], v[10:13]
	ds_read_b128 v[138:141], v101 offset:4096
	s_waitcnt lgkmcnt(9)
	v_mfma_f32_16x16x32_f16 v[78:81], v[142:145], v[146:149], v[78:81]
	v_mfma_f32_16x16x32_f16 v[62:65], v[142:145], v[150:153], v[62:65]
	v_mfma_f32_16x16x32_f16 v[34:37], v[142:145], v[154:157], v[34:37]
	v_mfma_f32_16x16x32_f16 v[2:5], v[142:145], v[158:161], v[2:5]
	ds_read_b128 v[142:145], v101 offset:5120
	s_add_i32 s7, s7, -1
	s_cmp_eq_u32 s7, 0
	s_cbranch_scc0 .Lg0_cloop
	s_waitcnt lgkmcnt(0)
	s_mul_i32 s24, s22, 0x3400
	s_lshl_b32 s28, s2, 6
	s_add_i32 s29, s20, s28
	s_and_b32 s30, s29, 0x7ff
	v_add_u32_e32 v98, s30, v102
	v_lshlrev_b32_e32 v98, 8, v98
	v_lshl_add_u32 v98, v120, 4, v98
	v_add_u32_e32 v99, 0x1000, v98
	v_add_u32_e32 v100, 0x2000, v98
	v_add_u32_e32 v101, 0x3000, v98
	v_mul_u32_u24_e32 v103, 0xd0, v102
	v_lshl_add_u32 v103, v120, 3, v103
	v_add_u32_e32 v103, s24, v103
	v_lshrrev_b32_e32 v0, 2, v1
	v_and_b32_e32 v1, 3, v1
	v_mul_u32_u24_e32 v102, 0xd0, v0
	v_lshl_add_u32 v102, v1, 4, v102
	v_add_u32_e32 v102, s24, v102
	v_lshlrev_b32_e32 v0, 11, v0
	v_lshl_add_u32 v0, v1, 4, v0
	s_lshl_b32 s31, s5, 7
	s_add_i32 s35, s31, 0
	s_and_b32 s35, s35, 0xff
	s_add_u32 s36, s12, s35
	s_addc_u32 s37, s13, 0
	s_add_i32 s35, s31, 64
	s_and_b32 s35, s35, 0xff
	s_add_u32 s38, s12, s35
	s_addc_u32 s39, s13, 0
	s_add_i32 s35, s31, 128
	s_and_b32 s35, s35, 0xff
	s_add_u32 s40, s12, s35
	s_addc_u32 s41, s13, 0
	s_add_i32 s35, s31, 192
	s_and_b32 s35, s35, 0xff
	s_add_u32 s42, s12, s35
	s_addc_u32 s43, s13, 0
	s_add_i32 s34, s25, s23
	s_sub_i32 s32, 0x400, s34
	s_ashr_i32 s32, s32, 4
	s_max_i32 s32, s32, 0
	s_min_i32 s32, s32, 6
	s_sub_i32 s33, 0x800, s34
	s_ashr_i32 s33, s33, 4
	s_max_i32 s33, s33, 0
	s_min_i32 s33, s33, 6
	s_cmp_eq_u32 s33, 0
	s_cbranch_scc1 .Lepi_noload
	global_load_dwordx4 v[108:111], v98, s[38:39]
	global_load_dwordx4 v[124:127], v99, s[38:39]
	global_load_dwordx4 v[140:143], v100, s[38:39]
	global_load_dwordx4 v[156:159], v101, s[38:39]
	global_load_dwordx4 v[104:107], v98, s[36:37]
	global_load_dwordx4 v[120:123], v99, s[36:37]
	global_load_dwordx4 v[136:139], v100, s[36:37]
	global_load_dwordx4 v[152:155], v101, s[36:37]
	global_load_dwordx4 v[116:119], v98, s[42:43]
	global_load_dwordx4 v[132:135], v99, s[42:43]
	global_load_dwordx4 v[148:151], v100, s[42:43]
	global_load_dwordx4 v[164:167], v101, s[42:43]
	global_load_dwordx4 v[112:115], v98, s[40:41]
	global_load_dwordx4 v[128:131], v99, s[40:41]
	global_load_dwordx4 v[144:147], v100, s[40:41]
	global_load_dwordx4 v[160:163], v101, s[40:41]
.Lepi_noload:
	s_barrier
	s_cmp_le_u32 s33, 5
	s_cbranch_scc1 .Lepi_v5
	s_waitcnt vmcnt(12)
	s_cmp_le_u32 s32, 5
	s_cbranch_scc1 .Lepi_r5
	v_mul_f32_e32 v108, 0x3e38aa3b, v108
	v_mul_f32_e32 v109, 0x3e38aa3b, v109
	v_mul_f32_e32 v110, 0x3e38aa3b, v110
	v_mul_f32_e32 v111, 0x3e38aa3b, v111
	v_mul_f32_e32 v124, 0x3e38aa3b, v124
	v_mul_f32_e32 v125, 0x3e38aa3b, v125
	v_mul_f32_e32 v126, 0x3e38aa3b, v126
	v_mul_f32_e32 v127, 0x3e38aa3b, v127
	v_mul_f32_e32 v140, 0x3e38aa3b, v140
	v_mul_f32_e32 v141, 0x3e38aa3b, v141
	v_mul_f32_e32 v142, 0x3e38aa3b, v142
	v_mul_f32_e32 v143, 0x3e38aa3b, v143
	v_mul_f32_e32 v156, 0x3e38aa3b, v156
	v_mul_f32_e32 v157, 0x3e38aa3b, v157
	v_mul_f32_e32 v158, 0x3e38aa3b, v158
	v_mul_f32_e32 v159, 0x3e38aa3b, v159
